# speedup vs baseline: 1.0218x; 1.0020x over previous
_Z11prep_kernelPKfPjPfS1_:
	s_load_dwordx4 s[4:7], s[0:1], 0x0
	s_and_b32 s3, s2, 7
	s_lshr_b32 s8, s2, 3
	s_lshr_b32 s9, s3, 1
	s_lshl_b32 s9, s9, 7
	s_lshl_b32 s8, s8, 1
	s_and_b32 s3, s3, 1
	s_add_i32 s2, s9, s8
	s_add_i32 s2, s2, s3
	v_or_b32_e32 v1, s2, v0
	v_cmp_eq_u32_e32 vcc, 0, v1
	s_and_saveexec_b64 s[8:9], vcc
	s_cbranch_execz .LBB0_2
	s_load_dwordx2 s[10:11], s[0:1], 0x18
	v_mov_b32_e32 v1, 0
	s_waitcnt lgkmcnt(0)
	global_store_dword v1, v1, s[10:11]
	global_store_dword v1, v1, s[10:11] offset:-4096
	global_store_dword v1, v1, s[10:11] offset:-4092
	global_store_dword v1, v1, s[10:11] offset:-4088
	global_store_dword v1, v1, s[10:11] offset:-4084
	global_store_dword v1, v1, s[10:11] offset:-4080
	global_store_dword v1, v1, s[10:11] offset:-4076
	global_store_dword v1, v1, s[10:11] offset:-4072
	global_store_dword v1, v1, s[10:11] offset:-4068
	global_store_dword v1, v1, s[10:11] offset:-4064
	global_store_dword v1, v1, s[10:11] offset:-4060
